# conversion loops of the projection-phase spare workgroups: counted wait (vmcnt 16) instead of the progressive 15..0 ladder, as already done in the mixer instance
# baseline (speedup 1.0000x reference)
.Lcvp0_a_ready:
	v_mul_f32_e32 v0, 0x42800000, v2
	v_mul_f32_e32 v131, 0x42800000, v6
	v_cvt_pk_fp8_f32 v130, v0, v131
	v_mul_f32_e32 v132, 0x42800000, v10
	v_mul_f32_e32 v133, 0x42800000, v14
	v_mul_f32_e32 v0, 0x42800000, v18
	v_cvt_pk_fp8_f32 v130, v132, v133 op_sel:[0,0,1]
	v_mul_f32_e32 v132, 0x42800000, v22
	v_cvt_pk_fp8_f32 v131, v0, v132
	v_mul_f32_e32 v133, 0x42800000, v26
	v_mul_f32_e32 v138, 0x42800000, v30
	v_mul_f32_e32 v0, 0x42800000, v34
	v_cvt_pk_fp8_f32 v131, v133, v138 op_sel:[0,0,1]
	v_mul_f32_e32 v133, 0x42800000, v38
	v_cvt_pk_fp8_f32 v132, v0, v133
	v_mul_f32_e32 v138, 0x42800000, v42
	v_mul_f32_e32 v139, 0x42800000, v46
	v_mul_f32_e32 v0, 0x42800000, v50
	v_cvt_pk_fp8_f32 v132, v138, v139 op_sel:[0,0,1]
	v_mul_f32_e32 v138, 0x42800000, v54
	v_cvt_pk_fp8_f32 v133, v0, v138
	v_mul_f32_e32 v139, 0x42800000, v58
	v_mul_f32_e32 v149, 0x42800000, v62
	v_mul_f32_e32 v0, 0x42800000, v3
	v_cvt_pk_fp8_f32 v133, v139, v149 op_sel:[0,0,1]
	v_mul_f32_e32 v138, 0x42800000, v31
	v_mul_f32_e32 v139, 0x42800000, v47
	v_mul_f32_e32 v149, 0x42800000, v63
	ds_write_b128 v144, v[130:133]
	v_mul_f32_e32 v131, 0x42800000, v7
	s_nop 0
	v_cvt_pk_fp8_f32 v130, v0, v131
	v_mul_f32_e32 v132, 0x42800000, v11
	v_mul_f32_e32 v133, 0x42800000, v15
	v_mul_f32_e32 v0, 0x42800000, v19
	v_cvt_pk_fp8_f32 v130, v132, v133 op_sel:[0,0,1]
	v_mul_f32_e32 v132, 0x42800000, v23
	v_cvt_pk_fp8_f32 v131, v0, v132
	v_mul_f32_e32 v133, 0x42800000, v27
	v_mul_f32_e32 v0, 0x42800000, v35
	v_cvt_pk_fp8_f32 v131, v133, v138 op_sel:[0,0,1]
	v_mul_f32_e32 v133, 0x42800000, v39
	v_cvt_pk_fp8_f32 v132, v0, v133
	v_mul_f32_e32 v138, 0x42800000, v43
	v_mul_f32_e32 v0, 0x42800000, v51
	v_cvt_pk_fp8_f32 v132, v138, v139 op_sel:[0,0,1]
	v_mul_f32_e32 v138, 0x42800000, v55
	v_cvt_pk_fp8_f32 v133, v0, v138
	v_mul_f32_e32 v139, 0x42800000, v59
	v_mul_f32_e32 v0, 0x42800000, v4
	v_mul_f32_e32 v138, 0x42800000, v32
	v_cvt_pk_fp8_f32 v133, v139, v149 op_sel:[0,0,1]
	v_mul_f32_e32 v139, 0x42800000, v48
	v_mul_f32_e32 v149, 0x42800000, v64
	s_cmp_lg_u32 s31, 0
	ds_write_b128 v144, v[130:133] offset:128
	v_mul_f32_e32 v131, 0x42800000, v8
	s_nop 0
	v_cvt_pk_fp8_f32 v130, v0, v131
	v_mul_f32_e32 v132, 0x42800000, v12
	v_mul_f32_e32 v133, 0x42800000, v16
	v_mul_f32_e32 v0, 0x42800000, v20
	v_cvt_pk_fp8_f32 v130, v132, v133 op_sel:[0,0,1]
	v_mul_f32_e32 v132, 0x42800000, v24
	v_cvt_pk_fp8_f32 v131, v0, v132
	v_mul_f32_e32 v133, 0x42800000, v28
	v_mul_f32_e32 v0, 0x42800000, v36
	v_cvt_pk_fp8_f32 v131, v133, v138 op_sel:[0,0,1]
	v_mul_f32_e32 v133, 0x42800000, v40
	v_cvt_pk_fp8_f32 v132, v0, v133
	v_mul_f32_e32 v138, 0x42800000, v44
	v_mul_f32_e32 v0, 0x42800000, v52
	v_cvt_pk_fp8_f32 v132, v138, v139 op_sel:[0,0,1]
	v_mul_f32_e32 v138, 0x42800000, v56
	v_cvt_pk_fp8_f32 v133, v0, v138
	v_mul_f32_e32 v139, 0x42800000, v60
	v_mul_f32_e32 v0, 0x42800000, v5
	v_mul_f32_e32 v138, 0x42800000, v33
	v_cvt_pk_fp8_f32 v133, v139, v149 op_sel:[0,0,1]
	v_mul_f32_e32 v139, 0x42800000, v49
	v_mul_f32_e32 v149, 0x42800000, v65
	s_cselect_b64 s[20:21], -1, 0
	ds_write_b128 v144, v[130:133] offset:256
	v_mul_f32_e32 v131, 0x42800000, v9
	s_nop 0
	v_cvt_pk_fp8_f32 v130, v0, v131
	v_mul_f32_e32 v132, 0x42800000, v13
	v_mul_f32_e32 v133, 0x42800000, v17
	v_mul_f32_e32 v0, 0x42800000, v21
	v_cvt_pk_fp8_f32 v130, v132, v133 op_sel:[0,0,1]
	v_mul_f32_e32 v132, 0x42800000, v25
	v_cvt_pk_fp8_f32 v131, v0, v132
	v_mul_f32_e32 v133, 0x42800000, v29
	v_mul_f32_e32 v0, 0x42800000, v37
	v_cvt_pk_fp8_f32 v131, v133, v138 op_sel:[0,0,1]
	v_mul_f32_e32 v133, 0x42800000, v41
	v_cvt_pk_fp8_f32 v132, v0, v133
	v_mul_f32_e32 v138, 0x42800000, v45
	v_mul_f32_e32 v0, 0x42800000, v53
	v_cvt_pk_fp8_f32 v132, v138, v139 op_sel:[0,0,1]
	v_mul_f32_e32 v138, 0x42800000, v57
	v_cvt_pk_fp8_f32 v133, v0, v138
	v_mul_f32_e32 v139, 0x42800000, v61
	v_add_u32_e32 v138, s8, v140
	s_cmp_eq_u32 s31, 0
	v_cvt_pk_fp8_f32 v133, v139, v149 op_sel:[0,0,1]
	ds_write_b128 v144, v[130:133] offset:384
	s_waitcnt lgkmcnt(0)
	s_barrier
	ds_read_b128 v[130:133], v145
	s_cbranch_scc1 .LBB0_586
	v_cmp_lt_i32_e32 vcc, s47, v138
	v_lshlrev_b32_e32 v0, 1, v138
	v_and_b32_e32 v139, 0x7f, v138
	s_and_saveexec_b64 s[6:7], vcc
	s_xor_b64 s[6:7], exec, s[6:7]
	v_add_u32_e32 v0, 0x7ffff800, v0
	v_and_b32_e32 v0, 0x7fffff00, v0
	v_or3_b32 v138, v139, v0, s64
	s_andn2_saveexec_b64 s[6:7], s[6:7]
	v_and_or_b32 v138, v0, s65, v139
	s_or_b64 exec, exec, s[6:7]

.LBB0_612:
	s_waitcnt vmcnt(0)
.Lcvp0_b_ready:
	v_mul_f32_e32 v0, 0x42800000, v70
	v_mul_f32_e32 v131, 0x42800000, v66
	s_nop 0
	v_cvt_pk_fp8_f32 v130, v0, v131
	v_mul_f32_e32 v132, 0x42800000, v78
	v_mul_f32_e32 v133, 0x42800000, v74
	v_mul_f32_e32 v0, 0x42800000, v86
	v_cvt_pk_fp8_f32 v130, v132, v133 op_sel:[0,0,1]
	v_mul_f32_e32 v132, 0x42800000, v82
	v_cvt_pk_fp8_f32 v131, v0, v132
	v_mul_f32_e32 v133, 0x42800000, v94
	v_mul_f32_e32 v138, 0x42800000, v90
	v_mul_f32_e32 v0, 0x42800000, v98
	v_cvt_pk_fp8_f32 v131, v133, v138 op_sel:[0,0,1]
	v_mul_f32_e32 v133, 0x42800000, v102
	v_cvt_pk_fp8_f32 v132, v0, v133
	v_mul_f32_e32 v138, 0x42800000, v106
	v_mul_f32_e32 v139, 0x42800000, v110
	v_mul_f32_e32 v0, 0x42800000, v114
	v_cvt_pk_fp8_f32 v132, v138, v139 op_sel:[0,0,1]
	v_mul_f32_e32 v138, 0x42800000, v118
	v_cvt_pk_fp8_f32 v133, v0, v138
	v_mul_f32_e32 v139, 0x42800000, v122
	v_mul_f32_e32 v149, 0x42800000, v126
	v_mul_f32_e32 v0, 0x42800000, v71
	v_cvt_pk_fp8_f32 v133, v139, v149 op_sel:[0,0,1]
	v_mul_f32_e32 v138, 0x42800000, v91
	v_mul_f32_e32 v139, 0x42800000, v111
	v_mul_f32_e32 v149, 0x42800000, v127
	ds_write_b128 v144, v[130:133] offset:32768
	v_mul_f32_e32 v131, 0x42800000, v67
	s_nop 0
	v_cvt_pk_fp8_f32 v130, v0, v131
	v_mul_f32_e32 v132, 0x42800000, v79
	v_mul_f32_e32 v133, 0x42800000, v75
	v_mul_f32_e32 v0, 0x42800000, v87
	v_cvt_pk_fp8_f32 v130, v132, v133 op_sel:[0,0,1]
	v_mul_f32_e32 v132, 0x42800000, v83
	v_cvt_pk_fp8_f32 v131, v0, v132
	v_mul_f32_e32 v133, 0x42800000, v95
	v_mul_f32_e32 v0, 0x42800000, v99
	v_cvt_pk_fp8_f32 v131, v133, v138 op_sel:[0,0,1]
	v_mul_f32_e32 v133, 0x42800000, v103
	v_cvt_pk_fp8_f32 v132, v0, v133
	v_mul_f32_e32 v138, 0x42800000, v107
	v_mul_f32_e32 v0, 0x42800000, v115
	v_cvt_pk_fp8_f32 v132, v138, v139 op_sel:[0,0,1]
	v_mul_f32_e32 v138, 0x42800000, v119
	v_cvt_pk_fp8_f32 v133, v0, v138
	v_mul_f32_e32 v139, 0x42800000, v123
	v_mul_f32_e32 v0, 0x42800000, v72
	v_mul_f32_e32 v138, 0x42800000, v92
	v_cvt_pk_fp8_f32 v133, v139, v149 op_sel:[0,0,1]
	v_mul_f32_e32 v139, 0x42800000, v112
	v_mul_f32_e32 v149, 0x42800000, v128
	s_cmp_lg_u32 s37, 0
	ds_write_b128 v144, v[130:133] offset:32896
	v_mul_f32_e32 v131, 0x42800000, v68
	s_nop 0
	v_cvt_pk_fp8_f32 v130, v0, v131
	v_mul_f32_e32 v132, 0x42800000, v80
	v_mul_f32_e32 v133, 0x42800000, v76
	v_mul_f32_e32 v0, 0x42800000, v88
	v_cvt_pk_fp8_f32 v130, v132, v133 op_sel:[0,0,1]
	v_mul_f32_e32 v132, 0x42800000, v84
	v_cvt_pk_fp8_f32 v131, v0, v132
	v_mul_f32_e32 v133, 0x42800000, v96
	v_mul_f32_e32 v0, 0x42800000, v100
	v_cvt_pk_fp8_f32 v131, v133, v138 op_sel:[0,0,1]
	v_mul_f32_e32 v133, 0x42800000, v104
	v_cvt_pk_fp8_f32 v132, v0, v133
	v_mul_f32_e32 v138, 0x42800000, v108
	v_mul_f32_e32 v0, 0x42800000, v116
	v_cvt_pk_fp8_f32 v132, v138, v139 op_sel:[0,0,1]
	v_mul_f32_e32 v138, 0x42800000, v120
	v_cvt_pk_fp8_f32 v133, v0, v138
	v_mul_f32_e32 v139, 0x42800000, v124
	v_mul_f32_e32 v0, 0x42800000, v73
	v_mul_f32_e32 v138, 0x42800000, v93
	v_cvt_pk_fp8_f32 v133, v139, v149 op_sel:[0,0,1]
	v_mul_f32_e32 v139, 0x42800000, v113
	v_mul_f32_e32 v149, 0x42800000, v129
	s_cselect_b64 s[18:19], -1, 0
	ds_write_b128 v144, v[130:133] offset:33024
	v_mul_f32_e32 v131, 0x42800000, v69
	s_nop 0
	v_cvt_pk_fp8_f32 v130, v0, v131
	v_mul_f32_e32 v132, 0x42800000, v81
	v_mul_f32_e32 v133, 0x42800000, v77
	v_mul_f32_e32 v0, 0x42800000, v89
	v_cvt_pk_fp8_f32 v130, v132, v133 op_sel:[0,0,1]
	v_mul_f32_e32 v132, 0x42800000, v85
	v_cvt_pk_fp8_f32 v131, v0, v132
	v_mul_f32_e32 v133, 0x42800000, v97
	v_mul_f32_e32 v0, 0x42800000, v101
	v_cvt_pk_fp8_f32 v131, v133, v138 op_sel:[0,0,1]
	v_mul_f32_e32 v133, 0x42800000, v105
	v_cvt_pk_fp8_f32 v132, v0, v133
	v_mul_f32_e32 v138, 0x42800000, v109
	v_mul_f32_e32 v0, 0x42800000, v117
	v_cvt_pk_fp8_f32 v132, v138, v139 op_sel:[0,0,1]
	v_mul_f32_e32 v138, 0x42800000, v121
	v_cvt_pk_fp8_f32 v133, v0, v138
	v_mul_f32_e32 v139, 0x42800000, v125
	v_add_u32_e32 v138, s12, v140
	s_cmp_eq_u32 s37, 0
	v_cvt_pk_fp8_f32 v133, v139, v149 op_sel:[0,0,1]
	ds_write_b128 v144, v[130:133] offset:33152
	s_waitcnt lgkmcnt(0)
	s_barrier
	ds_read_b128 v[130:133], v145 offset:32768
	s_cbranch_scc1 .LBB0_618
	v_cmp_lt_i32_e32 vcc, s47, v138
	v_lshlrev_b32_e32 v0, 1, v138
	v_and_b32_e32 v139, 0x7f, v138
	s_and_saveexec_b64 s[6:7], vcc
	s_xor_b64 s[6:7], exec, s[6:7]
	v_add_u32_e32 v0, 0x7ffff800, v0
	v_and_b32_e32 v0, 0x7fffff00, v0
	v_or3_b32 v138, v139, v0, s64
	s_andn2_saveexec_b64 s[6:7], s[6:7]
	v_and_or_b32 v138, v0, s65, v139
	s_or_b64 exec, exec, s[6:7]

.Lcvp1_a_ready:
	v_mul_f32_e32 v0, 0x42800000, v2
	v_mul_f32_e32 v131, 0x42800000, v6
	v_cvt_pk_fp8_f32 v130, v0, v131
	v_mul_f32_e32 v132, 0x42800000, v10
	v_mul_f32_e32 v133, 0x42800000, v14
	v_mul_f32_e32 v0, 0x42800000, v18
	v_cvt_pk_fp8_f32 v130, v132, v133 op_sel:[0,0,1]
	v_mul_f32_e32 v132, 0x42800000, v22
	v_cvt_pk_fp8_f32 v131, v0, v132
	v_mul_f32_e32 v133, 0x42800000, v26
	v_mul_f32_e32 v138, 0x42800000, v30
	v_mul_f32_e32 v0, 0x42800000, v34
	v_cvt_pk_fp8_f32 v131, v133, v138 op_sel:[0,0,1]
	v_mul_f32_e32 v133, 0x42800000, v38
	v_cvt_pk_fp8_f32 v132, v0, v133
	v_mul_f32_e32 v138, 0x42800000, v42
	v_mul_f32_e32 v139, 0x42800000, v46
	v_mul_f32_e32 v0, 0x42800000, v50
	v_cvt_pk_fp8_f32 v132, v138, v139 op_sel:[0,0,1]
	v_mul_f32_e32 v138, 0x42800000, v54
	v_cvt_pk_fp8_f32 v133, v0, v138
	v_mul_f32_e32 v139, 0x42800000, v58
	v_mul_f32_e32 v149, 0x42800000, v62
	v_mul_f32_e32 v0, 0x42800000, v3
	v_cvt_pk_fp8_f32 v133, v139, v149 op_sel:[0,0,1]
	v_mul_f32_e32 v138, 0x42800000, v31
	v_mul_f32_e32 v139, 0x42800000, v47
	v_mul_f32_e32 v149, 0x42800000, v63
	ds_write_b128 v144, v[130:133]
	v_mul_f32_e32 v131, 0x42800000, v7
	s_nop 0
	v_cvt_pk_fp8_f32 v130, v0, v131
	v_mul_f32_e32 v132, 0x42800000, v11
	v_mul_f32_e32 v133, 0x42800000, v15
	v_mul_f32_e32 v0, 0x42800000, v19
	v_cvt_pk_fp8_f32 v130, v132, v133 op_sel:[0,0,1]
	v_mul_f32_e32 v132, 0x42800000, v23
	v_cvt_pk_fp8_f32 v131, v0, v132
	v_mul_f32_e32 v133, 0x42800000, v27
	v_mul_f32_e32 v0, 0x42800000, v35
	v_cvt_pk_fp8_f32 v131, v133, v138 op_sel:[0,0,1]
	v_mul_f32_e32 v133, 0x42800000, v39
	v_cvt_pk_fp8_f32 v132, v0, v133
	v_mul_f32_e32 v138, 0x42800000, v43
	v_mul_f32_e32 v0, 0x42800000, v51
	v_cvt_pk_fp8_f32 v132, v138, v139 op_sel:[0,0,1]
	v_mul_f32_e32 v138, 0x42800000, v55
	v_cvt_pk_fp8_f32 v133, v0, v138
	v_mul_f32_e32 v139, 0x42800000, v59
	v_mul_f32_e32 v0, 0x42800000, v4
	v_mul_f32_e32 v138, 0x42800000, v32
	v_cvt_pk_fp8_f32 v133, v139, v149 op_sel:[0,0,1]
	v_mul_f32_e32 v139, 0x42800000, v48
	v_mul_f32_e32 v149, 0x42800000, v64
	s_cmp_lg_u32 s36, 0
	ds_write_b128 v144, v[130:133] offset:128
	v_mul_f32_e32 v131, 0x42800000, v8
	s_nop 0
	v_cvt_pk_fp8_f32 v130, v0, v131
	v_mul_f32_e32 v132, 0x42800000, v12
	v_mul_f32_e32 v133, 0x42800000, v16
	v_mul_f32_e32 v0, 0x42800000, v20
	v_cvt_pk_fp8_f32 v130, v132, v133 op_sel:[0,0,1]
	v_mul_f32_e32 v132, 0x42800000, v24
	v_cvt_pk_fp8_f32 v131, v0, v132
	v_mul_f32_e32 v133, 0x42800000, v28
	v_mul_f32_e32 v0, 0x42800000, v36
	v_cvt_pk_fp8_f32 v131, v133, v138 op_sel:[0,0,1]
	v_mul_f32_e32 v133, 0x42800000, v40
	v_cvt_pk_fp8_f32 v132, v0, v133
	v_mul_f32_e32 v138, 0x42800000, v44
	v_mul_f32_e32 v0, 0x42800000, v52
	v_cvt_pk_fp8_f32 v132, v138, v139 op_sel:[0,0,1]
	v_mul_f32_e32 v138, 0x42800000, v56
	v_cvt_pk_fp8_f32 v133, v0, v138
	v_mul_f32_e32 v139, 0x42800000, v60
	v_mul_f32_e32 v0, 0x42800000, v5
	v_mul_f32_e32 v138, 0x42800000, v33
	v_cvt_pk_fp8_f32 v133, v139, v149 op_sel:[0,0,1]
	v_mul_f32_e32 v139, 0x42800000, v49
	v_mul_f32_e32 v149, 0x42800000, v65
	s_cselect_b64 s[20:21], -1, 0
	ds_write_b128 v144, v[130:133] offset:256
	v_mul_f32_e32 v131, 0x42800000, v9
	s_nop 0
	v_cvt_pk_fp8_f32 v130, v0, v131
	v_mul_f32_e32 v132, 0x42800000, v13
	v_mul_f32_e32 v133, 0x42800000, v17
	v_mul_f32_e32 v0, 0x42800000, v21
	v_cvt_pk_fp8_f32 v130, v132, v133 op_sel:[0,0,1]
	v_mul_f32_e32 v132, 0x42800000, v25
	v_cvt_pk_fp8_f32 v131, v0, v132
	v_mul_f32_e32 v133, 0x42800000, v29
	v_mul_f32_e32 v0, 0x42800000, v37
	v_cvt_pk_fp8_f32 v131, v133, v138 op_sel:[0,0,1]
	v_mul_f32_e32 v133, 0x42800000, v41
	v_cvt_pk_fp8_f32 v132, v0, v133
	v_mul_f32_e32 v138, 0x42800000, v45
	v_mul_f32_e32 v0, 0x42800000, v53
	v_cvt_pk_fp8_f32 v132, v138, v139 op_sel:[0,0,1]
	v_mul_f32_e32 v138, 0x42800000, v57
	v_cvt_pk_fp8_f32 v133, v0, v138
	v_mul_f32_e32 v139, 0x42800000, v61
	v_add_u32_e32 v138, s8, v140
	s_cmp_eq_u32 s36, 0
	v_cvt_pk_fp8_f32 v133, v139, v149 op_sel:[0,0,1]
	ds_write_b128 v144, v[130:133] offset:384
	s_waitcnt lgkmcnt(0)
	s_barrier
	ds_read_b128 v[130:133], v145
	s_cbranch_scc1 .LBB0_661
	v_cmp_lt_i32_e32 vcc, s47, v138
	v_lshlrev_b32_e32 v0, 1, v138
	v_and_b32_e32 v139, 0x7f, v138
	s_and_saveexec_b64 s[6:7], vcc
	s_xor_b64 s[6:7], exec, s[6:7]
	v_add_u32_e32 v0, 0x7ffff800, v0
	v_and_b32_e32 v0, 0x7fffff00, v0
	v_or3_b32 v138, v139, v0, s64
	s_andn2_saveexec_b64 s[6:7], s[6:7]
	v_and_or_b32 v138, v0, s65, v139
	s_or_b64 exec, exec, s[6:7]

.LBB0_687:
	s_waitcnt vmcnt(0)
.Lcvp1_b_ready:
	v_mul_f32_e32 v0, 0x42800000, v70
	v_mul_f32_e32 v131, 0x42800000, v66
	s_nop 0
	v_cvt_pk_fp8_f32 v130, v0, v131
	v_mul_f32_e32 v132, 0x42800000, v78
	v_mul_f32_e32 v133, 0x42800000, v74
	v_mul_f32_e32 v0, 0x42800000, v86
	v_cvt_pk_fp8_f32 v130, v132, v133 op_sel:[0,0,1]
	v_mul_f32_e32 v132, 0x42800000, v82
	v_cvt_pk_fp8_f32 v131, v0, v132
	v_mul_f32_e32 v133, 0x42800000, v94
	v_mul_f32_e32 v138, 0x42800000, v90
	v_mul_f32_e32 v0, 0x42800000, v98
	v_cvt_pk_fp8_f32 v131, v133, v138 op_sel:[0,0,1]
	v_mul_f32_e32 v133, 0x42800000, v102
	v_cvt_pk_fp8_f32 v132, v0, v133
	v_mul_f32_e32 v138, 0x42800000, v106
	v_mul_f32_e32 v139, 0x42800000, v110
	v_mul_f32_e32 v0, 0x42800000, v114
	v_cvt_pk_fp8_f32 v132, v138, v139 op_sel:[0,0,1]
	v_mul_f32_e32 v138, 0x42800000, v118
	v_cvt_pk_fp8_f32 v133, v0, v138
	v_mul_f32_e32 v139, 0x42800000, v122
	v_mul_f32_e32 v149, 0x42800000, v126
	v_mul_f32_e32 v0, 0x42800000, v71
	v_cvt_pk_fp8_f32 v133, v139, v149 op_sel:[0,0,1]
	v_mul_f32_e32 v138, 0x42800000, v91
	v_mul_f32_e32 v139, 0x42800000, v111
	v_mul_f32_e32 v149, 0x42800000, v127
	ds_write_b128 v144, v[130:133] offset:32768
	v_mul_f32_e32 v131, 0x42800000, v67
	s_nop 0
	v_cvt_pk_fp8_f32 v130, v0, v131
	v_mul_f32_e32 v132, 0x42800000, v79
	v_mul_f32_e32 v133, 0x42800000, v75
	v_mul_f32_e32 v0, 0x42800000, v87
	v_cvt_pk_fp8_f32 v130, v132, v133 op_sel:[0,0,1]
	v_mul_f32_e32 v132, 0x42800000, v83
	v_cvt_pk_fp8_f32 v131, v0, v132
	v_mul_f32_e32 v133, 0x42800000, v95
	v_mul_f32_e32 v0, 0x42800000, v99
	v_cvt_pk_fp8_f32 v131, v133, v138 op_sel:[0,0,1]
	v_mul_f32_e32 v133, 0x42800000, v103
	v_cvt_pk_fp8_f32 v132, v0, v133
	v_mul_f32_e32 v138, 0x42800000, v107
	v_mul_f32_e32 v0, 0x42800000, v115
	v_cvt_pk_fp8_f32 v132, v138, v139 op_sel:[0,0,1]
	v_mul_f32_e32 v138, 0x42800000, v119
	v_cvt_pk_fp8_f32 v133, v0, v138
	v_mul_f32_e32 v139, 0x42800000, v123
	v_mul_f32_e32 v0, 0x42800000, v72
	v_mul_f32_e32 v138, 0x42800000, v92
	v_cvt_pk_fp8_f32 v133, v139, v149 op_sel:[0,0,1]
	v_mul_f32_e32 v139, 0x42800000, v112
	v_mul_f32_e32 v149, 0x42800000, v128
	s_cmp_lg_u32 s40, 0
	ds_write_b128 v144, v[130:133] offset:32896
	v_mul_f32_e32 v131, 0x42800000, v68
	s_nop 0
	v_cvt_pk_fp8_f32 v130, v0, v131
	v_mul_f32_e32 v132, 0x42800000, v80
	v_mul_f32_e32 v133, 0x42800000, v76
	v_mul_f32_e32 v0, 0x42800000, v88
	v_cvt_pk_fp8_f32 v130, v132, v133 op_sel:[0,0,1]
	v_mul_f32_e32 v132, 0x42800000, v84
	v_cvt_pk_fp8_f32 v131, v0, v132
	v_mul_f32_e32 v133, 0x42800000, v96
	v_mul_f32_e32 v0, 0x42800000, v100
	v_cvt_pk_fp8_f32 v131, v133, v138 op_sel:[0,0,1]
	v_mul_f32_e32 v133, 0x42800000, v104
	v_cvt_pk_fp8_f32 v132, v0, v133
	v_mul_f32_e32 v138, 0x42800000, v108
	v_mul_f32_e32 v0, 0x42800000, v116
	v_cvt_pk_fp8_f32 v132, v138, v139 op_sel:[0,0,1]
	v_mul_f32_e32 v138, 0x42800000, v120
	v_cvt_pk_fp8_f32 v133, v0, v138
	v_mul_f32_e32 v139, 0x42800000, v124
	v_mul_f32_e32 v0, 0x42800000, v73
	v_mul_f32_e32 v138, 0x42800000, v93
	v_cvt_pk_fp8_f32 v133, v139, v149 op_sel:[0,0,1]
	v_mul_f32_e32 v139, 0x42800000, v113
	v_mul_f32_e32 v149, 0x42800000, v129
	s_cselect_b64 s[18:19], -1, 0
	ds_write_b128 v144, v[130:133] offset:33024
	v_mul_f32_e32 v131, 0x42800000, v69
	s_nop 0
	v_cvt_pk_fp8_f32 v130, v0, v131
	v_mul_f32_e32 v132, 0x42800000, v81
	v_mul_f32_e32 v133, 0x42800000, v77
	v_mul_f32_e32 v0, 0x42800000, v89
	v_cvt_pk_fp8_f32 v130, v132, v133 op_sel:[0,0,1]
	v_mul_f32_e32 v132, 0x42800000, v85
	v_cvt_pk_fp8_f32 v131, v0, v132
	v_mul_f32_e32 v133, 0x42800000, v97
	v_mul_f32_e32 v0, 0x42800000, v101
	v_cvt_pk_fp8_f32 v131, v133, v138 op_sel:[0,0,1]
	v_mul_f32_e32 v133, 0x42800000, v105
	v_cvt_pk_fp8_f32 v132, v0, v133
	v_mul_f32_e32 v138, 0x42800000, v109
	v_mul_f32_e32 v0, 0x42800000, v117
	v_cvt_pk_fp8_f32 v132, v138, v139 op_sel:[0,0,1]
	v_mul_f32_e32 v138, 0x42800000, v121
	v_cvt_pk_fp8_f32 v133, v0, v138
	v_mul_f32_e32 v139, 0x42800000, v125
	v_add_u32_e32 v138, s12, v140
	s_cmp_eq_u32 s40, 0
	v_cvt_pk_fp8_f32 v133, v139, v149 op_sel:[0,0,1]
	ds_write_b128 v144, v[130:133] offset:33152
	s_waitcnt lgkmcnt(0)
	s_barrier
	ds_read_b128 v[130:133], v145 offset:32768
	s_cbranch_scc1 .LBB0_693
	v_cmp_lt_i32_e32 vcc, s47, v138
	v_lshlrev_b32_e32 v0, 1, v138
	v_and_b32_e32 v139, 0x7f, v138
	s_and_saveexec_b64 s[6:7], vcc
	s_xor_b64 s[6:7], exec, s[6:7]
	v_add_u32_e32 v0, 0x7ffff800, v0
	v_and_b32_e32 v0, 0x7fffff00, v0
	v_or3_b32 v138, v139, v0, s64
	s_andn2_saveexec_b64 s[6:7], s[6:7]
	v_and_or_b32 v138, v0, s65, v139
	s_or_b64 exec, exec, s[6:7]

.Lcvp3_a_ready:
	v_mul_f32_e32 v0, 0x42800000, v2
	v_mul_f32_e32 v131, 0x42800000, v6
	v_cvt_pk_fp8_f32 v130, v0, v131
	v_mul_f32_e32 v132, 0x42800000, v10
	v_mul_f32_e32 v133, 0x42800000, v14
	v_mul_f32_e32 v0, 0x42800000, v18
	v_cvt_pk_fp8_f32 v130, v132, v133 op_sel:[0,0,1]
	v_mul_f32_e32 v132, 0x42800000, v22
	v_cvt_pk_fp8_f32 v131, v0, v132
	v_mul_f32_e32 v133, 0x42800000, v26
	v_mul_f32_e32 v138, 0x42800000, v30
	v_mul_f32_e32 v0, 0x42800000, v34
	v_cvt_pk_fp8_f32 v131, v133, v138 op_sel:[0,0,1]
	v_mul_f32_e32 v133, 0x42800000, v38
	v_cvt_pk_fp8_f32 v132, v0, v133
	v_mul_f32_e32 v138, 0x42800000, v42
	v_mul_f32_e32 v139, 0x42800000, v46
	v_mul_f32_e32 v0, 0x42800000, v50
	v_cvt_pk_fp8_f32 v132, v138, v139 op_sel:[0,0,1]
	v_mul_f32_e32 v138, 0x42800000, v54
	v_cvt_pk_fp8_f32 v133, v0, v138
	v_mul_f32_e32 v139, 0x42800000, v58
	v_mul_f32_e32 v149, 0x42800000, v62
	v_mul_f32_e32 v0, 0x42800000, v3
	v_cvt_pk_fp8_f32 v133, v139, v149 op_sel:[0,0,1]
	v_mul_f32_e32 v138, 0x42800000, v31
	v_mul_f32_e32 v139, 0x42800000, v47
	v_mul_f32_e32 v149, 0x42800000, v63
	ds_write_b128 v144, v[130:133]
	v_mul_f32_e32 v131, 0x42800000, v7
	s_nop 0
	v_cvt_pk_fp8_f32 v130, v0, v131
	v_mul_f32_e32 v132, 0x42800000, v11
	v_mul_f32_e32 v133, 0x42800000, v15
	v_mul_f32_e32 v0, 0x42800000, v19
	v_cvt_pk_fp8_f32 v130, v132, v133 op_sel:[0,0,1]
	v_mul_f32_e32 v132, 0x42800000, v23
	v_cvt_pk_fp8_f32 v131, v0, v132
	v_mul_f32_e32 v133, 0x42800000, v27
	v_mul_f32_e32 v0, 0x42800000, v35
	v_cvt_pk_fp8_f32 v131, v133, v138 op_sel:[0,0,1]
	v_mul_f32_e32 v133, 0x42800000, v39
	v_cvt_pk_fp8_f32 v132, v0, v133
	v_mul_f32_e32 v138, 0x42800000, v43
	v_mul_f32_e32 v0, 0x42800000, v51
	v_cvt_pk_fp8_f32 v132, v138, v139 op_sel:[0,0,1]
	v_mul_f32_e32 v138, 0x42800000, v55
	v_cvt_pk_fp8_f32 v133, v0, v138
	v_mul_f32_e32 v139, 0x42800000, v59
	v_mul_f32_e32 v0, 0x42800000, v4
	v_mul_f32_e32 v138, 0x42800000, v32
	v_cvt_pk_fp8_f32 v133, v139, v149 op_sel:[0,0,1]
	v_mul_f32_e32 v139, 0x42800000, v48
	v_mul_f32_e32 v149, 0x42800000, v64
	s_cmp_lg_u32 s34, 0
	ds_write_b128 v144, v[130:133] offset:128
	v_mul_f32_e32 v131, 0x42800000, v8
	s_nop 0
	v_cvt_pk_fp8_f32 v130, v0, v131
	v_mul_f32_e32 v132, 0x42800000, v12
	v_mul_f32_e32 v133, 0x42800000, v16
	v_mul_f32_e32 v0, 0x42800000, v20
	v_cvt_pk_fp8_f32 v130, v132, v133 op_sel:[0,0,1]
	v_mul_f32_e32 v132, 0x42800000, v24
	v_cvt_pk_fp8_f32 v131, v0, v132
	v_mul_f32_e32 v133, 0x42800000, v28
	v_mul_f32_e32 v0, 0x42800000, v36
	v_cvt_pk_fp8_f32 v131, v133, v138 op_sel:[0,0,1]
	v_mul_f32_e32 v133, 0x42800000, v40
	v_cvt_pk_fp8_f32 v132, v0, v133
	v_mul_f32_e32 v138, 0x42800000, v44
	v_mul_f32_e32 v0, 0x42800000, v52
	v_cvt_pk_fp8_f32 v132, v138, v139 op_sel:[0,0,1]
	v_mul_f32_e32 v138, 0x42800000, v56
	v_cvt_pk_fp8_f32 v133, v0, v138
	v_mul_f32_e32 v139, 0x42800000, v60
	v_mul_f32_e32 v0, 0x42800000, v5
	v_mul_f32_e32 v138, 0x42800000, v33
	v_cvt_pk_fp8_f32 v133, v139, v149 op_sel:[0,0,1]
	v_mul_f32_e32 v139, 0x42800000, v49
	v_mul_f32_e32 v149, 0x42800000, v65
	s_cselect_b64 s[20:21], -1, 0
	ds_write_b128 v144, v[130:133] offset:256
	v_mul_f32_e32 v131, 0x42800000, v9
	s_nop 0
	v_cvt_pk_fp8_f32 v130, v0, v131
	v_mul_f32_e32 v132, 0x42800000, v13
	v_mul_f32_e32 v133, 0x42800000, v17
	v_mul_f32_e32 v0, 0x42800000, v21
	v_cvt_pk_fp8_f32 v130, v132, v133 op_sel:[0,0,1]
	v_mul_f32_e32 v132, 0x42800000, v25
	v_cvt_pk_fp8_f32 v131, v0, v132
	v_mul_f32_e32 v133, 0x42800000, v29
	v_mul_f32_e32 v0, 0x42800000, v37
	v_cvt_pk_fp8_f32 v131, v133, v138 op_sel:[0,0,1]
	v_mul_f32_e32 v133, 0x42800000, v41
	v_cvt_pk_fp8_f32 v132, v0, v133
	v_mul_f32_e32 v138, 0x42800000, v45
	v_mul_f32_e32 v0, 0x42800000, v53
	v_cvt_pk_fp8_f32 v132, v138, v139 op_sel:[0,0,1]
	v_mul_f32_e32 v138, 0x42800000, v57
	v_cvt_pk_fp8_f32 v133, v0, v138
	v_mul_f32_e32 v139, 0x42800000, v61
	v_add_u32_e32 v138, s8, v140
	s_cmp_eq_u32 s34, 0
	v_cvt_pk_fp8_f32 v133, v139, v149 op_sel:[0,0,1]
	ds_write_b128 v144, v[130:133] offset:384
	s_waitcnt lgkmcnt(0)
	s_barrier
	ds_read_b128 v[130:133], v145
	s_cbranch_scc1 .LBB0_1429
	v_cmp_lt_i32_e32 vcc, s47, v138
	v_lshlrev_b32_e32 v0, 1, v138
	v_and_b32_e32 v139, 0x7f, v138
	s_and_saveexec_b64 s[6:7], vcc
	s_xor_b64 s[6:7], exec, s[6:7]
	v_add_u32_e32 v0, 0x7ffff800, v0
	v_and_b32_e32 v0, 0x7fffff00, v0
	v_or3_b32 v138, v139, v0, s64
	s_andn2_saveexec_b64 s[6:7], s[6:7]
	v_and_or_b32 v138, v0, s65, v139
	s_or_b64 exec, exec, s[6:7]

.LBB0_1455:
	s_waitcnt vmcnt(0)
.Lcvp3_b_ready:
	v_mul_f32_e32 v0, 0x42800000, v70
	v_mul_f32_e32 v131, 0x42800000, v66
	s_nop 0
	v_cvt_pk_fp8_f32 v130, v0, v131
	v_mul_f32_e32 v132, 0x42800000, v78
	v_mul_f32_e32 v133, 0x42800000, v74
	v_mul_f32_e32 v0, 0x42800000, v86
	v_cvt_pk_fp8_f32 v130, v132, v133 op_sel:[0,0,1]
	v_mul_f32_e32 v132, 0x42800000, v82
	v_cvt_pk_fp8_f32 v131, v0, v132
	v_mul_f32_e32 v133, 0x42800000, v94
	v_mul_f32_e32 v138, 0x42800000, v90
	v_mul_f32_e32 v0, 0x42800000, v98
	v_cvt_pk_fp8_f32 v131, v133, v138 op_sel:[0,0,1]
	v_mul_f32_e32 v133, 0x42800000, v102
	v_cvt_pk_fp8_f32 v132, v0, v133
	v_mul_f32_e32 v138, 0x42800000, v106
	v_mul_f32_e32 v139, 0x42800000, v110
	v_mul_f32_e32 v0, 0x42800000, v114
	v_cvt_pk_fp8_f32 v132, v138, v139 op_sel:[0,0,1]
	v_mul_f32_e32 v138, 0x42800000, v118
	v_cvt_pk_fp8_f32 v133, v0, v138
	v_mul_f32_e32 v139, 0x42800000, v122
	v_mul_f32_e32 v149, 0x42800000, v126
	v_mul_f32_e32 v0, 0x42800000, v71
	v_cvt_pk_fp8_f32 v133, v139, v149 op_sel:[0,0,1]
	v_mul_f32_e32 v138, 0x42800000, v91
	v_mul_f32_e32 v139, 0x42800000, v111
	v_mul_f32_e32 v149, 0x42800000, v127
	ds_write_b128 v144, v[130:133] offset:32768
	v_mul_f32_e32 v131, 0x42800000, v67
	s_nop 0
	v_cvt_pk_fp8_f32 v130, v0, v131
	v_mul_f32_e32 v132, 0x42800000, v79
	v_mul_f32_e32 v133, 0x42800000, v75
	v_mul_f32_e32 v0, 0x42800000, v87
	v_cvt_pk_fp8_f32 v130, v132, v133 op_sel:[0,0,1]
	v_mul_f32_e32 v132, 0x42800000, v83
	v_cvt_pk_fp8_f32 v131, v0, v132
	v_mul_f32_e32 v133, 0x42800000, v95
	v_mul_f32_e32 v0, 0x42800000, v99
	v_cvt_pk_fp8_f32 v131, v133, v138 op_sel:[0,0,1]
	v_mul_f32_e32 v133, 0x42800000, v103
	v_cvt_pk_fp8_f32 v132, v0, v133
	v_mul_f32_e32 v138, 0x42800000, v107
	v_mul_f32_e32 v0, 0x42800000, v115
	v_cvt_pk_fp8_f32 v132, v138, v139 op_sel:[0,0,1]
	v_mul_f32_e32 v138, 0x42800000, v119
	v_cvt_pk_fp8_f32 v133, v0, v138
	v_mul_f32_e32 v139, 0x42800000, v123
	v_mul_f32_e32 v0, 0x42800000, v72
	v_mul_f32_e32 v138, 0x42800000, v92
	v_cvt_pk_fp8_f32 v133, v139, v149 op_sel:[0,0,1]
	v_mul_f32_e32 v139, 0x42800000, v112
	v_mul_f32_e32 v149, 0x42800000, v128
	s_cmp_lg_u32 s37, 0
	ds_write_b128 v144, v[130:133] offset:32896
	v_mul_f32_e32 v131, 0x42800000, v68
	s_nop 0
	v_cvt_pk_fp8_f32 v130, v0, v131
	v_mul_f32_e32 v132, 0x42800000, v80
	v_mul_f32_e32 v133, 0x42800000, v76
	v_mul_f32_e32 v0, 0x42800000, v88
	v_cvt_pk_fp8_f32 v130, v132, v133 op_sel:[0,0,1]
	v_mul_f32_e32 v132, 0x42800000, v84
	v_cvt_pk_fp8_f32 v131, v0, v132
	v_mul_f32_e32 v133, 0x42800000, v96
	v_mul_f32_e32 v0, 0x42800000, v100
	v_cvt_pk_fp8_f32 v131, v133, v138 op_sel:[0,0,1]
	v_mul_f32_e32 v133, 0x42800000, v104
	v_cvt_pk_fp8_f32 v132, v0, v133
	v_mul_f32_e32 v138, 0x42800000, v108
	v_mul_f32_e32 v0, 0x42800000, v116
	v_cvt_pk_fp8_f32 v132, v138, v139 op_sel:[0,0,1]
	v_mul_f32_e32 v138, 0x42800000, v120
	v_cvt_pk_fp8_f32 v133, v0, v138
	v_mul_f32_e32 v139, 0x42800000, v124
	v_mul_f32_e32 v0, 0x42800000, v73
	v_mul_f32_e32 v138, 0x42800000, v93
	v_cvt_pk_fp8_f32 v133, v139, v149 op_sel:[0,0,1]
	v_mul_f32_e32 v139, 0x42800000, v113
	v_mul_f32_e32 v149, 0x42800000, v129
	s_cselect_b64 s[18:19], -1, 0
	ds_write_b128 v144, v[130:133] offset:33024
	v_mul_f32_e32 v131, 0x42800000, v69
	s_nop 0
	v_cvt_pk_fp8_f32 v130, v0, v131
	v_mul_f32_e32 v132, 0x42800000, v81
	v_mul_f32_e32 v133, 0x42800000, v77
	v_mul_f32_e32 v0, 0x42800000, v89
	v_cvt_pk_fp8_f32 v130, v132, v133 op_sel:[0,0,1]
	v_mul_f32_e32 v132, 0x42800000, v85
	v_cvt_pk_fp8_f32 v131, v0, v132
	v_mul_f32_e32 v133, 0x42800000, v97
	v_mul_f32_e32 v0, 0x42800000, v101
	v_cvt_pk_fp8_f32 v131, v133, v138 op_sel:[0,0,1]
	v_mul_f32_e32 v133, 0x42800000, v105
	v_cvt_pk_fp8_f32 v132, v0, v133
	v_mul_f32_e32 v138, 0x42800000, v109
	v_mul_f32_e32 v0, 0x42800000, v117
	v_cvt_pk_fp8_f32 v132, v138, v139 op_sel:[0,0,1]
	v_mul_f32_e32 v138, 0x42800000, v121
	v_cvt_pk_fp8_f32 v133, v0, v138
	v_mul_f32_e32 v139, 0x42800000, v125
	v_add_u32_e32 v138, s12, v140
	s_cmp_eq_u32 s37, 0
	v_cvt_pk_fp8_f32 v133, v139, v149 op_sel:[0,0,1]
	ds_write_b128 v144, v[130:133] offset:33152
	s_waitcnt lgkmcnt(0)
	s_barrier
	ds_read_b128 v[130:133], v145 offset:32768
	s_cbranch_scc1 .LBB0_1461
	v_cmp_lt_i32_e32 vcc, s47, v138
	v_lshlrev_b32_e32 v0, 1, v138
	v_and_b32_e32 v139, 0x7f, v138
	s_and_saveexec_b64 s[6:7], vcc
	s_xor_b64 s[6:7], exec, s[6:7]
	v_add_u32_e32 v0, 0x7ffff800, v0
	v_and_b32_e32 v0, 0x7fffff00, v0
	v_or3_b32 v138, v139, v0, s64
	s_andn2_saveexec_b64 s[6:7], s[6:7]
	v_and_or_b32 v138, v0, s65, v139
	s_or_b64 exec, exec, s[6:7]
